# speedup vs baseline: 1.0148x; 1.0020x over previous
.LBB0_10:
	v_lshlrev_b32_e32 v2, 4, v0
	v_lshrrev_b32_e32 v3, 4, v0
	v_lshlrev_b32_e32 v3, 19, v3
	v_bfe_u32 v4, v0, 3, 1
	v_lshl_or_b32 v3, v4, 7, v3
	v_and_b32_e32 v4, 7, v0
	v_lshl_or_b32 v3, v4, 3, v3
	s_lshl_b32 s8, s3, 14
	s_lshl_b32 s9, s3, 9
	s_waitcnt lgkmcnt(0)
	s_add_u32 s6, s6, s8
	s_addc_u32 s7, s7, 0
	s_add_u32 s4, s4, s9
	s_addc_u32 s5, s5, 0
	s_add_u32 s8, s6, 0x1000
	s_addc_u32 s9, s7, 0
	s_add_u32 s10, s6, 0x2000
	s_addc_u32 s11, s7, 0
	s_add_u32 s12, s6, 0x3000
	s_addc_u32 s13, s7, 0
	global_load_dwordx4 v[8:11], v2, s[6:7] nt
	global_load_dwordx4 v[12:15], v2, s[8:9] nt
	global_load_dwordx4 v[16:19], v2, s[10:11] nt
	global_load_dwordx4 v[20:23], v2, s[12:13] nt
	s_waitcnt vmcnt(3)
	v_cvt_pk_bf16_f32 v8, v8, v9
	v_cvt_pk_bf16_f32 v9, v10, v11
	global_store_dwordx2 v3, v[8:9], s[4:5]
	s_waitcnt vmcnt(3)
	v_cvt_pk_bf16_f32 v12, v12, v13
	v_cvt_pk_bf16_f32 v13, v14, v15
	global_store_dwordx2 v3, v[12:13], s[4:5] offset:64
	s_waitcnt vmcnt(3)
	v_cvt_pk_bf16_f32 v16, v16, v17
	v_cvt_pk_bf16_f32 v17, v18, v19
	global_store_dwordx2 v3, v[16:17], s[4:5] offset:256
	s_waitcnt vmcnt(3)
	v_cvt_pk_bf16_f32 v20, v20, v21
	v_cvt_pk_bf16_f32 v21, v22, v23
	global_store_dwordx2 v3, v[20:21], s[4:5] offset:320
	s_endpgm

.LBB4_15:
	ds_read_b128 v[156:159], v138
	ds_read_b128 v[160:163], v139
	ds_read_b128 v[164:167], v140
	ds_read_b128 v[168:171], v141
	ds_read_b128 v[172:175], v142
	ds_read_b128 v[176:179], v143
	ds_read_b128 v[180:183], v144
	ds_read_b128 v[184:187], v145
	s_add_i32 s40, s37, -2
	s_min_u32 s41, s37, 0x83
	s_add_i32 s42, s2, 0xffffc000
	s_mov_b32 m0, s18
	s_add_i32 s60, s16, s37
	s_add_i32 s60, s60, -1
	s_cmp_lt_u32 s60, 16
	s_cselect_b32 s61, s54, s55
	s_cselect_b32 s62, 0x20000, s63
	s_lshl_b32 s60, s60, 13
	s_add_i32 s56, s61, s60
	s_add_i32 s57, s56, s62
	s_add_i32 s58, s57, s62
	s_add_i32 s59, s58, s62
	buffer_load_dwordx4 v1, s[8:11], s56 offen lds
	s_mov_b32 m0, s38
	s_nop 0
	buffer_load_dwordx4 v1, s[8:11], s57 offen lds
	s_mov_b32 m0, s19
	s_nop 0
	buffer_load_dwordx4 v1, s[8:11], s58 offen lds
	s_mov_b32 m0, s39
	s_nop 0
	buffer_load_dwordx4 v1, s[8:11], s59 offen lds
	ds_read_b64_tr_b16 v[188:189], v146
	ds_read_b64_tr_b16 v[190:191], v146 offset:512
	ds_read_b64_tr_b16 v[192:193], v147
	ds_read_b64_tr_b16 v[194:195], v147 offset:512
	ds_read_b64_tr_b16 v[196:197], v146 offset:4096
	ds_read_b64_tr_b16 v[198:199], v146 offset:4608
	ds_read_b64_tr_b16 v[200:201], v147 offset:4096
	ds_read_b64_tr_b16 v[202:203], v147 offset:4608
	ds_read_b64_tr_b16 v[204:205], v222
	ds_read_b64_tr_b16 v[206:207], v222 offset:512
	ds_read_b64_tr_b16 v[208:209], v223
	ds_read_b64_tr_b16 v[210:211], v223 offset:512
	ds_read_b64_tr_b16 v[212:213], v222 offset:4096
	ds_read_b64_tr_b16 v[214:215], v222 offset:4608
	ds_read_b64_tr_b16 v[216:217], v223 offset:4096
	ds_read_b64_tr_b16 v[218:219], v223 offset:4608
	s_waitcnt lgkmcnt(15)
	s_barrier
	s_waitcnt lgkmcnt(0)
	s_setprio 1
	s_waitcnt lgkmcnt(7)
	v_mfma_f32_16x16x32_bf16 v[126:129], v[188:191], v[156:159], v[126:129]
	v_mfma_f32_16x16x32_bf16 v[94:97], v[188:191], v[164:167], v[94:97]
	s_waitcnt lgkmcnt(6)
	v_mfma_f32_16x16x32_bf16 v[122:125], v[192:195], v[156:159], v[122:125]
	v_mfma_f32_16x16x32_bf16 v[90:93], v[192:195], v[164:167], v[90:93]
	s_waitcnt lgkmcnt(3)
	v_mfma_f32_16x16x32_bf16 v[118:121], v[204:207], v[156:159], v[118:121]
	v_mfma_f32_16x16x32_bf16 v[86:89], v[204:207], v[164:167], v[86:89]
	s_waitcnt lgkmcnt(2)
	v_mfma_f32_16x16x32_bf16 v[114:117], v[208:211], v[156:159], v[114:117]
	v_mfma_f32_16x16x32_bf16 v[82:85], v[208:211], v[164:167], v[82:85]
	v_mfma_f32_16x16x32_bf16 v[126:129], v[196:199], v[160:163], v[126:129]
	v_mfma_f32_16x16x32_bf16 v[94:97], v[196:199], v[168:171], v[94:97]
	v_mfma_f32_16x16x32_bf16 v[122:125], v[200:203], v[160:163], v[122:125]
	v_mfma_f32_16x16x32_bf16 v[90:93], v[200:203], v[168:171], v[90:93]
	s_waitcnt lgkmcnt(1)
	v_mfma_f32_16x16x32_bf16 v[118:121], v[212:215], v[160:163], v[118:121]
	v_mfma_f32_16x16x32_bf16 v[86:89], v[212:215], v[168:171], v[86:89]
	s_waitcnt lgkmcnt(0)
	v_mfma_f32_16x16x32_bf16 v[114:117], v[216:219], v[160:163], v[114:117]
	v_mfma_f32_16x16x32_bf16 v[82:85], v[216:219], v[168:171], v[82:85]
	s_setprio 0
	s_setprio 1
	v_mfma_f32_16x16x32_bf16 v[62:65], v[188:191], v[172:175], v[62:65]
	v_mfma_f32_16x16x32_bf16 v[34:37], v[188:191], v[180:183], v[34:37]
	v_mfma_f32_16x16x32_bf16 v[58:61], v[192:195], v[172:175], v[58:61]
	v_mfma_f32_16x16x32_bf16 v[30:33], v[192:195], v[180:183], v[30:33]
	v_mfma_f32_16x16x32_bf16 v[54:57], v[204:207], v[172:175], v[54:57]
	v_mfma_f32_16x16x32_bf16 v[22:25], v[204:207], v[180:183], v[22:25]
	v_mfma_f32_16x16x32_bf16 v[50:53], v[208:211], v[172:175], v[50:53]
	v_mfma_f32_16x16x32_bf16 v[18:21], v[208:211], v[180:183], v[18:21]
	v_mfma_f32_16x16x32_bf16 v[62:65], v[196:199], v[176:179], v[62:65]
	v_mfma_f32_16x16x32_bf16 v[34:37], v[196:199], v[184:187], v[34:37]
	v_mfma_f32_16x16x32_bf16 v[58:61], v[200:203], v[176:179], v[58:61]
	v_mfma_f32_16x16x32_bf16 v[30:33], v[200:203], v[184:187], v[30:33]
	v_mfma_f32_16x16x32_bf16 v[54:57], v[212:215], v[176:179], v[54:57]
	v_mfma_f32_16x16x32_bf16 v[22:25], v[212:215], v[184:187], v[22:25]
	v_mfma_f32_16x16x32_bf16 v[50:53], v[216:219], v[176:179], v[50:53]
	v_mfma_f32_16x16x32_bf16 v[18:21], v[216:219], v[184:187], v[18:21]
	s_setprio 0
	s_barrier
	s_lshl_b32 s42, s41, 18
	s_or_b32 s43, s42, s23
	s_mov_b32 m0, s17
	s_lshl_b32 s43, s43, 1
	buffer_load_dwordx4 v130, s[4:7], s43 offen lds
	s_mov_b32 m0, s22
	s_or_b32 s42, s42, s24
	buffer_load_dwordx4 v133, s[4:7], s43 offen lds
	s_lshl_b32 s42, s42, 1
	s_mov_b32 m0, s25
	s_nop 0
	buffer_load_dwordx4 v130, s[4:7], s42 offen lds
	s_mov_b32 m0, s26
	s_nop 0
	buffer_load_dwordx4 v133, s[4:7], s42 offen lds
	ds_read_b64_tr_b16 v[188:189], v146 offset:16384
	ds_read_b64_tr_b16 v[190:191], v146 offset:16896
	ds_read_b64_tr_b16 v[192:193], v147 offset:16384
	ds_read_b64_tr_b16 v[194:195], v147 offset:16896
	ds_read_b64_tr_b16 v[196:197], v146 offset:20480
	ds_read_b64_tr_b16 v[198:199], v146 offset:20992
	ds_read_b64_tr_b16 v[200:201], v147 offset:20480
	ds_read_b64_tr_b16 v[202:203], v147 offset:20992
	ds_read_b64_tr_b16 v[204:205], v222 offset:16384
	ds_read_b64_tr_b16 v[206:207], v222 offset:16896
	ds_read_b64_tr_b16 v[208:209], v223 offset:16384
	ds_read_b64_tr_b16 v[210:211], v223 offset:16896
	ds_read_b64_tr_b16 v[212:213], v222 offset:20480
	ds_read_b64_tr_b16 v[214:215], v222 offset:20992
	ds_read_b64_tr_b16 v[216:217], v223 offset:20480
	ds_read_b64_tr_b16 v[218:219], v223 offset:20992
	s_waitcnt lgkmcnt(0)
	s_waitcnt vmcnt(4)
	s_barrier
	s_setprio 1
	s_waitcnt lgkmcnt(7)
	v_mfma_f32_16x16x32_bf16 v[110:113], v[188:191], v[156:159], v[110:113]
	v_mfma_f32_16x16x32_bf16 v[78:81], v[188:191], v[164:167], v[78:81]
	s_waitcnt lgkmcnt(6)
	v_mfma_f32_16x16x32_bf16 v[106:109], v[192:195], v[156:159], v[106:109]
	v_mfma_f32_16x16x32_bf16 v[74:77], v[192:195], v[164:167], v[74:77]
	s_waitcnt lgkmcnt(3)
	v_mfma_f32_16x16x32_bf16 v[102:105], v[204:207], v[156:159], v[102:105]
	v_mfma_f32_16x16x32_bf16 v[70:73], v[204:207], v[164:167], v[70:73]
	s_waitcnt lgkmcnt(2)
	v_mfma_f32_16x16x32_bf16 v[98:101], v[208:211], v[156:159], v[98:101]
	v_mfma_f32_16x16x32_bf16 v[66:69], v[208:211], v[164:167], v[66:69]
	v_mfma_f32_16x16x32_bf16 v[110:113], v[196:199], v[160:163], v[110:113]
	v_mfma_f32_16x16x32_bf16 v[78:81], v[196:199], v[168:171], v[78:81]
	v_mfma_f32_16x16x32_bf16 v[106:109], v[200:203], v[160:163], v[106:109]
	v_mfma_f32_16x16x32_bf16 v[74:77], v[200:203], v[168:171], v[74:77]
	s_waitcnt lgkmcnt(1)
	v_mfma_f32_16x16x32_bf16 v[102:105], v[212:215], v[160:163], v[102:105]
	v_mfma_f32_16x16x32_bf16 v[70:73], v[212:215], v[168:171], v[70:73]
	s_waitcnt lgkmcnt(0)
	v_mfma_f32_16x16x32_bf16 v[98:101], v[216:219], v[160:163], v[98:101]
	v_mfma_f32_16x16x32_bf16 v[66:69], v[216:219], v[168:171], v[66:69]
	s_setprio 0
	s_setprio 1
	v_mfma_f32_16x16x32_bf16 v[46:49], v[188:191], v[172:175], v[46:49]
	v_mfma_f32_16x16x32_bf16 v[10:13], v[188:191], v[180:183], v[10:13]
	v_mfma_f32_16x16x32_bf16 v[38:41], v[192:195], v[172:175], v[38:41]
	v_mfma_f32_16x16x32_bf16 v[2:5], v[192:195], v[180:183], v[2:5]
	v_mfma_f32_16x16x32_bf16 v[26:29], v[204:207], v[172:175], v[26:29]
	v_mfma_f32_16x16x32_bf16 v[14:17], v[204:207], v[180:183], v[14:17]
	v_mfma_f32_16x16x32_bf16 v[42:45], v[208:211], v[172:175], v[42:45]
	v_mfma_f32_16x16x32_bf16 v[6:9], v[208:211], v[180:183], v[6:9]
	v_mfma_f32_16x16x32_bf16 v[46:49], v[196:199], v[176:179], v[46:49]
	v_mfma_f32_16x16x32_bf16 v[10:13], v[196:199], v[184:187], v[10:13]
	v_mfma_f32_16x16x32_bf16 v[38:41], v[200:203], v[176:179], v[38:41]
	v_mfma_f32_16x16x32_bf16 v[2:5], v[200:203], v[184:187], v[2:5]
	v_mfma_f32_16x16x32_bf16 v[26:29], v[212:215], v[176:179], v[26:29]
	v_mfma_f32_16x16x32_bf16 v[14:17], v[212:215], v[184:187], v[14:17]
	v_mfma_f32_16x16x32_bf16 v[42:45], v[216:219], v[176:179], v[42:45]
	v_mfma_f32_16x16x32_bf16 v[6:9], v[216:219], v[184:187], v[6:9]
	s_setprio 0
	s_barrier
	ds_read_b128 v[156:159], v148
	ds_read_b128 v[160:163], v149
	ds_read_b128 v[164:167], v150
	ds_read_b128 v[168:171], v151
	ds_read_b128 v[172:175], v152
	ds_read_b128 v[176:179], v153
	ds_read_b128 v[180:183], v154
	ds_read_b128 v[184:187], v155
	s_lshl_b32 s41, s41, 16
	s_or_b32 s42, s41, s28
	s_mov_b32 m0, s3
	s_lshl_b32 s42, s42, 1
	s_min_u32 s60, s37, 0x83
	s_add_i32 s60, s60, s16
	s_cmp_lt_u32 s60, 16
	s_cselect_b32 s61, s54, s55
	s_cselect_b32 s62, 0x20000, s63
	s_lshl_b32 s60, s60, 13
	s_add_i32 s56, s61, s60
	s_add_i32 s57, s56, s62
	s_add_i32 s58, s57, s62
	s_add_i32 s59, s58, s62
	buffer_load_dwordx4 v1, s[8:11], s56 offen lds
	s_mov_b32 m0, s27
	s_or_b32 s41, s41, s29
	buffer_load_dwordx4 v1, s[8:11], s57 offen lds
	s_lshl_b32 s41, s41, 1
	s_mov_b32 m0, s30
	s_nop 0
	buffer_load_dwordx4 v1, s[8:11], s58 offen lds
	s_mov_b32 m0, s31
	s_nop 0
	buffer_load_dwordx4 v1, s[8:11], s59 offen lds
	ds_read_b64_tr_b16 v[188:189], v146 offset:32768
	ds_read_b64_tr_b16 v[190:191], v146 offset:33280
	ds_read_b64_tr_b16 v[192:193], v147 offset:32768
	ds_read_b64_tr_b16 v[194:195], v147 offset:33280
	ds_read_b64_tr_b16 v[196:197], v146 offset:36864
	ds_read_b64_tr_b16 v[198:199], v146 offset:37376
	ds_read_b64_tr_b16 v[200:201], v147 offset:36864
	ds_read_b64_tr_b16 v[202:203], v147 offset:37376
	ds_read_b64_tr_b16 v[204:205], v222 offset:32768
	ds_read_b64_tr_b16 v[206:207], v222 offset:33280
	ds_read_b64_tr_b16 v[208:209], v223 offset:32768
	ds_read_b64_tr_b16 v[210:211], v223 offset:33280
	ds_read_b64_tr_b16 v[212:213], v222 offset:36864
	ds_read_b64_tr_b16 v[214:215], v222 offset:37376
	ds_read_b64_tr_b16 v[216:217], v223 offset:36864
	ds_read_b64_tr_b16 v[218:219], v223 offset:37376
	s_waitcnt lgkmcnt(15)
	s_barrier
	s_waitcnt lgkmcnt(0)
	s_setprio 1
	s_waitcnt lgkmcnt(7)
	v_mfma_f32_16x16x32_bf16 v[126:129], v[188:191], v[156:159], v[126:129]
	v_mfma_f32_16x16x32_bf16 v[94:97], v[188:191], v[164:167], v[94:97]
	s_waitcnt lgkmcnt(6)
	v_mfma_f32_16x16x32_bf16 v[122:125], v[192:195], v[156:159], v[122:125]
	v_mfma_f32_16x16x32_bf16 v[90:93], v[192:195], v[164:167], v[90:93]
	s_waitcnt lgkmcnt(3)
	v_mfma_f32_16x16x32_bf16 v[118:121], v[204:207], v[156:159], v[118:121]
	v_mfma_f32_16x16x32_bf16 v[86:89], v[204:207], v[164:167], v[86:89]
	s_waitcnt lgkmcnt(2)
	v_mfma_f32_16x16x32_bf16 v[114:117], v[208:211], v[156:159], v[114:117]
	v_mfma_f32_16x16x32_bf16 v[82:85], v[208:211], v[164:167], v[82:85]
	v_mfma_f32_16x16x32_bf16 v[126:129], v[196:199], v[160:163], v[126:129]
	v_mfma_f32_16x16x32_bf16 v[94:97], v[196:199], v[168:171], v[94:97]
	v_mfma_f32_16x16x32_bf16 v[122:125], v[200:203], v[160:163], v[122:125]
	v_mfma_f32_16x16x32_bf16 v[90:93], v[200:203], v[168:171], v[90:93]
	s_waitcnt lgkmcnt(1)
	v_mfma_f32_16x16x32_bf16 v[118:121], v[212:215], v[160:163], v[118:121]
	v_mfma_f32_16x16x32_bf16 v[86:89], v[212:215], v[168:171], v[86:89]
	s_waitcnt lgkmcnt(0)
	v_mfma_f32_16x16x32_bf16 v[114:117], v[216:219], v[160:163], v[114:117]
	v_mfma_f32_16x16x32_bf16 v[82:85], v[216:219], v[168:171], v[82:85]
	s_setprio 0
	s_setprio 1
	v_mfma_f32_16x16x32_bf16 v[62:65], v[188:191], v[172:175], v[62:65]
	v_mfma_f32_16x16x32_bf16 v[34:37], v[188:191], v[180:183], v[34:37]
	v_mfma_f32_16x16x32_bf16 v[58:61], v[192:195], v[172:175], v[58:61]
	v_mfma_f32_16x16x32_bf16 v[30:33], v[192:195], v[180:183], v[30:33]
	v_mfma_f32_16x16x32_bf16 v[54:57], v[204:207], v[172:175], v[54:57]
	v_mfma_f32_16x16x32_bf16 v[22:25], v[204:207], v[180:183], v[22:25]
	v_mfma_f32_16x16x32_bf16 v[50:53], v[208:211], v[172:175], v[50:53]
	v_mfma_f32_16x16x32_bf16 v[18:21], v[208:211], v[180:183], v[18:21]
	v_mfma_f32_16x16x32_bf16 v[62:65], v[196:199], v[176:179], v[62:65]
	v_mfma_f32_16x16x32_bf16 v[34:37], v[196:199], v[184:187], v[34:37]
	v_mfma_f32_16x16x32_bf16 v[58:61], v[200:203], v[176:179], v[58:61]
	v_mfma_f32_16x16x32_bf16 v[30:33], v[200:203], v[184:187], v[30:33]
	v_mfma_f32_16x16x32_bf16 v[54:57], v[212:215], v[176:179], v[54:57]
	v_mfma_f32_16x16x32_bf16 v[22:25], v[212:215], v[184:187], v[22:25]
	v_mfma_f32_16x16x32_bf16 v[50:53], v[216:219], v[176:179], v[50:53]
	v_mfma_f32_16x16x32_bf16 v[18:21], v[216:219], v[184:187], v[18:21]
	s_setprio 0
	s_barrier
	s_min_u32 s41, s40, 0x80
	s_lshl_b32 s41, s41, 18
	s_add_i32 s41, s41, 0xc0000
	s_or_b32 s42, s41, s23
	s_mov_b32 m0, s33
	s_lshl_b32 s42, s42, 1
	buffer_load_dwordx4 v130, s[4:7], s42 offen lds
	s_mov_b32 m0, s34
	s_or_b32 s41, s41, s24
	buffer_load_dwordx4 v133, s[4:7], s42 offen lds
	s_lshl_b32 s41, s41, 1
	s_mov_b32 m0, s35
	s_nop 0
	buffer_load_dwordx4 v130, s[4:7], s41 offen lds
	s_mov_b32 m0, s36
	s_nop 0
	buffer_load_dwordx4 v133, s[4:7], s41 offen lds
	ds_read_b64_tr_b16 v[188:189], v146 offset:49152
	ds_read_b64_tr_b16 v[190:191], v146 offset:49664
	ds_read_b64_tr_b16 v[192:193], v147 offset:49152
	ds_read_b64_tr_b16 v[194:195], v147 offset:49664
	ds_read_b64_tr_b16 v[196:197], v146 offset:53248
	ds_read_b64_tr_b16 v[198:199], v146 offset:53760
	ds_read_b64_tr_b16 v[200:201], v147 offset:53248
	ds_read_b64_tr_b16 v[202:203], v147 offset:53760
	ds_read_b64_tr_b16 v[204:205], v222 offset:49152
	ds_read_b64_tr_b16 v[206:207], v222 offset:49664
	ds_read_b64_tr_b16 v[208:209], v223 offset:49152
	ds_read_b64_tr_b16 v[210:211], v223 offset:49664
	ds_read_b64_tr_b16 v[212:213], v222 offset:53248
	ds_read_b64_tr_b16 v[214:215], v222 offset:53760
	ds_read_b64_tr_b16 v[216:217], v223 offset:53248
	ds_read_b64_tr_b16 v[218:219], v223 offset:53760
	s_waitcnt lgkmcnt(0)
	s_waitcnt vmcnt(4)
	s_barrier
	s_setprio 1
	s_waitcnt lgkmcnt(7)
	v_mfma_f32_16x16x32_bf16 v[110:113], v[188:191], v[156:159], v[110:113]
	v_mfma_f32_16x16x32_bf16 v[78:81], v[188:191], v[164:167], v[78:81]
	s_waitcnt lgkmcnt(6)
	v_mfma_f32_16x16x32_bf16 v[106:109], v[192:195], v[156:159], v[106:109]
	v_mfma_f32_16x16x32_bf16 v[74:77], v[192:195], v[164:167], v[74:77]
	s_waitcnt lgkmcnt(3)
	v_mfma_f32_16x16x32_bf16 v[102:105], v[204:207], v[156:159], v[102:105]
	v_mfma_f32_16x16x32_bf16 v[70:73], v[204:207], v[164:167], v[70:73]
	s_waitcnt lgkmcnt(2)
	v_mfma_f32_16x16x32_bf16 v[98:101], v[208:211], v[156:159], v[98:101]
	v_mfma_f32_16x16x32_bf16 v[66:69], v[208:211], v[164:167], v[66:69]
	v_mfma_f32_16x16x32_bf16 v[110:113], v[196:199], v[160:163], v[110:113]
	v_mfma_f32_16x16x32_bf16 v[78:81], v[196:199], v[168:171], v[78:81]
	v_mfma_f32_16x16x32_bf16 v[106:109], v[200:203], v[160:163], v[106:109]
	v_mfma_f32_16x16x32_bf16 v[74:77], v[200:203], v[168:171], v[74:77]
	s_waitcnt lgkmcnt(1)
	v_mfma_f32_16x16x32_bf16 v[102:105], v[212:215], v[160:163], v[102:105]
	v_mfma_f32_16x16x32_bf16 v[70:73], v[212:215], v[168:171], v[70:73]
	s_waitcnt lgkmcnt(0)
	v_mfma_f32_16x16x32_bf16 v[98:101], v[216:219], v[160:163], v[98:101]
	v_mfma_f32_16x16x32_bf16 v[66:69], v[216:219], v[168:171], v[66:69]
	s_setprio 0
	s_setprio 1
	v_mfma_f32_16x16x32_bf16 v[46:49], v[188:191], v[172:175], v[46:49]
	v_mfma_f32_16x16x32_bf16 v[10:13], v[188:191], v[180:183], v[10:13]
	v_mfma_f32_16x16x32_bf16 v[38:41], v[192:195], v[172:175], v[38:41]
	v_mfma_f32_16x16x32_bf16 v[2:5], v[192:195], v[180:183], v[2:5]
	v_mfma_f32_16x16x32_bf16 v[26:29], v[204:207], v[172:175], v[26:29]
	v_mfma_f32_16x16x32_bf16 v[14:17], v[204:207], v[180:183], v[14:17]
	v_mfma_f32_16x16x32_bf16 v[42:45], v[208:211], v[172:175], v[42:45]
	v_mfma_f32_16x16x32_bf16 v[6:9], v[208:211], v[180:183], v[6:9]
	v_mfma_f32_16x16x32_bf16 v[46:49], v[196:199], v[176:179], v[46:49]
	v_mfma_f32_16x16x32_bf16 v[10:13], v[196:199], v[184:187], v[10:13]
	v_mfma_f32_16x16x32_bf16 v[38:41], v[200:203], v[176:179], v[38:41]
	v_mfma_f32_16x16x32_bf16 v[2:5], v[200:203], v[184:187], v[2:5]
	v_mfma_f32_16x16x32_bf16 v[26:29], v[212:215], v[176:179], v[26:29]
	v_mfma_f32_16x16x32_bf16 v[14:17], v[212:215], v[184:187], v[14:17]
	v_mfma_f32_16x16x32_bf16 v[42:45], v[216:219], v[176:179], v[42:45]
	v_mfma_f32_16x16x32_bf16 v[6:9], v[216:219], v[184:187], v[6:9]
	s_setprio 0
	s_barrier
	s_add_i32 s41, s16, s37
	s_add_i32 s44, s41, -2
	s_cmpk_lt_u32 s40, 0x82
	s_cselect_b64 s[42:43], -1, 0
	s_cmp_gt_i32 s44, 13
	s_cselect_b64 s[44:45], -1, 0
	s_and_b64 s[42:43], s[42:43], s[44:45]
	s_andn2_b64 vcc, exec, s[42:43]
	s_cbranch_vccnz .LBB4_14
	s_add_i32 s41, s41, -16
	s_and_b32 s41, s41, 62
	s_cmp_lg_u32 s41, 0
	s_cbranch_scc1 .LBB4_14
	ds_read2_b32 v[156:157], v137 offset1:16
	ds_read2_b32 v[158:159], v137 offset0:128 offset1:144
	s_waitcnt lgkmcnt(1)
	v_pk_mul_f32 v[128:129], v[156:157], v[128:129] op_sel_hi:[0,1]
	v_pk_mul_f32 v[126:127], v[156:157], v[126:127] op_sel_hi:[0,1]
	v_pk_mul_f32 v[124:125], v[156:157], v[124:125] op_sel_hi:[0,1]
	v_pk_mul_f32 v[122:123], v[156:157], v[122:123] op_sel_hi:[0,1]
	v_pk_mul_f32 v[120:121], v[156:157], v[120:121] op_sel_hi:[0,1]
	v_pk_mul_f32 v[118:119], v[156:157], v[118:119] op_sel_hi:[0,1]
	v_pk_mul_f32 v[116:117], v[156:157], v[116:117] op_sel_hi:[0,1]
	v_pk_mul_f32 v[114:115], v[156:157], v[114:115] op_sel_hi:[0,1]
	v_pk_mul_f32 v[112:113], v[156:157], v[112:113] op_sel_hi:[0,1]
	v_pk_mul_f32 v[110:111], v[156:157], v[110:111] op_sel_hi:[0,1]
	v_pk_mul_f32 v[108:109], v[156:157], v[108:109] op_sel_hi:[0,1]
	v_pk_mul_f32 v[106:107], v[156:157], v[106:107] op_sel_hi:[0,1]
	v_pk_mul_f32 v[104:105], v[156:157], v[104:105] op_sel_hi:[0,1]
	v_pk_mul_f32 v[102:103], v[156:157], v[102:103] op_sel_hi:[0,1]
	v_pk_mul_f32 v[100:101], v[156:157], v[100:101] op_sel_hi:[0,1]
	v_pk_mul_f32 v[98:99], v[156:157], v[98:99] op_sel_hi:[0,1]
	v_mov_b32_e32 v156, v157
	v_pk_mul_f32 v[96:97], v[156:157], v[96:97] op_sel_hi:[0,1]
	v_pk_mul_f32 v[94:95], v[156:157], v[94:95] op_sel_hi:[0,1]
	v_pk_mul_f32 v[92:93], v[156:157], v[92:93] op_sel_hi:[0,1]
	v_pk_mul_f32 v[90:91], v[156:157], v[90:91] op_sel_hi:[0,1]
	v_pk_mul_f32 v[88:89], v[156:157], v[88:89] op_sel_hi:[0,1]
	v_pk_mul_f32 v[86:87], v[156:157], v[86:87] op_sel_hi:[0,1]
	v_pk_mul_f32 v[84:85], v[156:157], v[84:85] op_sel_hi:[0,1]
	v_pk_mul_f32 v[82:83], v[156:157], v[82:83] op_sel_hi:[0,1]
	v_pk_mul_f32 v[80:81], v[156:157], v[80:81] op_sel_hi:[0,1]
	v_pk_mul_f32 v[78:79], v[156:157], v[78:79] op_sel_hi:[0,1]
	v_pk_mul_f32 v[76:77], v[156:157], v[76:77] op_sel_hi:[0,1]
	v_pk_mul_f32 v[74:75], v[156:157], v[74:75] op_sel_hi:[0,1]
	v_pk_mul_f32 v[72:73], v[156:157], v[72:73] op_sel_hi:[0,1]
	v_pk_mul_f32 v[70:71], v[156:157], v[70:71] op_sel_hi:[0,1]
	v_pk_mul_f32 v[68:69], v[156:157], v[68:69] op_sel_hi:[0,1]
	v_pk_mul_f32 v[66:67], v[156:157], v[66:67] op_sel_hi:[0,1]
	s_waitcnt lgkmcnt(0)
	v_mov_b32_e32 v156, v159
	v_pk_mul_f32 v[64:65], v[158:159], v[64:65] op_sel_hi:[0,1]
	v_pk_mul_f32 v[62:63], v[158:159], v[62:63] op_sel_hi:[0,1]
	v_pk_mul_f32 v[60:61], v[158:159], v[60:61] op_sel_hi:[0,1]
	v_pk_mul_f32 v[58:59], v[158:159], v[58:59] op_sel_hi:[0,1]
	v_pk_mul_f32 v[56:57], v[158:159], v[56:57] op_sel_hi:[0,1]
	v_pk_mul_f32 v[54:55], v[158:159], v[54:55] op_sel_hi:[0,1]
	v_pk_mul_f32 v[52:53], v[158:159], v[52:53] op_sel_hi:[0,1]
	v_pk_mul_f32 v[50:51], v[158:159], v[50:51] op_sel_hi:[0,1]
	v_pk_mul_f32 v[48:49], v[158:159], v[48:49] op_sel_hi:[0,1]
	v_pk_mul_f32 v[46:47], v[158:159], v[46:47] op_sel_hi:[0,1]
	v_pk_mul_f32 v[40:41], v[158:159], v[40:41] op_sel_hi:[0,1]
	v_pk_mul_f32 v[38:39], v[158:159], v[38:39] op_sel_hi:[0,1]
	v_pk_mul_f32 v[28:29], v[158:159], v[28:29] op_sel_hi:[0,1]
	v_pk_mul_f32 v[26:27], v[158:159], v[26:27] op_sel_hi:[0,1]
	v_pk_mul_f32 v[44:45], v[158:159], v[44:45] op_sel_hi:[0,1]
	v_pk_mul_f32 v[42:43], v[158:159], v[42:43] op_sel_hi:[0,1]
	v_pk_mul_f32 v[36:37], v[156:157], v[36:37] op_sel_hi:[0,1]
	v_pk_mul_f32 v[34:35], v[156:157], v[34:35] op_sel_hi:[0,1]
	v_pk_mul_f32 v[32:33], v[156:157], v[32:33] op_sel_hi:[0,1]
	v_pk_mul_f32 v[30:31], v[156:157], v[30:31] op_sel_hi:[0,1]
	v_pk_mul_f32 v[24:25], v[156:157], v[24:25] op_sel_hi:[0,1]
	v_pk_mul_f32 v[22:23], v[156:157], v[22:23] op_sel_hi:[0,1]
	v_pk_mul_f32 v[20:21], v[156:157], v[20:21] op_sel_hi:[0,1]
	v_pk_mul_f32 v[18:19], v[156:157], v[18:19] op_sel_hi:[0,1]
	v_pk_mul_f32 v[12:13], v[156:157], v[12:13] op_sel_hi:[0,1]
	v_pk_mul_f32 v[10:11], v[156:157], v[10:11] op_sel_hi:[0,1]
	v_pk_mul_f32 v[4:5], v[156:157], v[4:5] op_sel_hi:[0,1]
	v_pk_mul_f32 v[2:3], v[156:157], v[2:3] op_sel_hi:[0,1]
	v_pk_mul_f32 v[16:17], v[156:157], v[16:17] op_sel_hi:[0,1]
	v_pk_mul_f32 v[14:15], v[156:157], v[14:15] op_sel_hi:[0,1]
	v_pk_mul_f32 v[8:9], v[156:157], v[8:9] op_sel_hi:[0,1]
	v_pk_mul_f32 v[6:7], v[156:157], v[6:7] op_sel_hi:[0,1]
	s_branch .LBB4_14
